# gdn scan rewritten: shadow half issues LDS-DMA, scan half rotated 32-MFMA pipeline
# speedup vs baseline: 1.0034x; 1.0034x over previous
; DI int tidx() { int t = threadIdx.x & 255; asm volatile("" : "+v"(t)); return t; }
; DI void gdn_scan_seq(const Params& p, int bh16, char* ldsf) {
;   const int tid = tidx(), lane = tid & 63, wv = tid >> 6;
;   const float* glp = (const float*)(p.ws + WS_GL) + bh16 * 128;
;   const char* wf = (const char*)(p.ws + WS_WF) + (size_t)bh16 * 128 * 16384 + tid * 16;
;   const char* kf = (const char*)p.out + 32 * MiB + (size_t)bh16 * 128 * 16384 + tid * 16;
;   const char* uf = (const char*)(p.ws + WS_UF) + (size_t)bh16 * 128 * 16384 + (size_t)(wv * 64 + lane) * 32;
;   char* scp = p.ws + WS_SC + (size_t)bh16 * 128 * 32768 + (size_t)wv * 8192 + lane * 16;
;   float* glt = (float*)(ldsf + 2 * LDS_BYTES + 64);
;   if (tid < 128) glt[tid] = glp[tid];
;     ...
;   f32x16 S[4];
; #pragma unroll
;   for (int m = 0; m < 4; ++m)
; #pragma unroll
;     for (int r = 0; r < 16; ++r) S[m][r] = 0.f;
;   asm volatile("s_waitcnt vmcnt(0)" ::: "memory");
;   __syncthreads();
;   SCAN_ISSUE(0, 0); SCAN_ISSUE(1, 1);
; DI void phase_mixer(const Params& p, int bid, int nb, char* lds, char* ctl, char* ldsf) {
;     ...
;   if (bid < 32) { if (vb == 0) gdn_scan_seq(p, bid >> 1, ldsf); else { __syncthreads(); for (int k = 0; k < 128; ++k) { __builtin_amdgcn_s_barrier(); asm volatile("" ::: "memory"); } __syncthreads(); } }
.LBB0_1207:
	s_or_b64 exec, exec, s[0:1]
	v_mov_b32_e32 v135, v206
	s_waitcnt lgkmcnt(0)
	s_barrier
	s_and_saveexec_b64 s[0:1], s[6:7]
	s_cbranch_execz .LBB0_1227
	s_movk_i32 s2, 0xff
	v_cmp_lt_u32_e32 vcc, s2, v207
	s_and_saveexec_b64 s[2:3], vcc
	s_xor_b64 s[6:7], exec, s[2:3]
	s_cbranch_execz .LBB0_1212
	v_readlane_b32 s2, v250, 0
	v_lshrrev_b32_e32 v0, 6, v206
	v_and_b32_e32 v1, 63, v206
	v_lshlrev_b32_e32 v7, 12, v0
	v_lshl_or_b32 v8, v1, 4, v7
	v_add_u32_e32 v9, 0x400, v8
	v_add_u32_e32 v10, 0x800, v8
	v_add_u32_e32 v11, 0xc00, v8
	v_lshlrev_b32_e32 v3, 11, v0
	v_lshl_or_b32 v3, v1, 5, v3
	v_or_b32_e32 v4, 16, v3
	v_or_b32_e32 v5, 0x2000, v3
	v_or_b32_e32 v6, 0x2010, v3
	v_readfirstlane_b32 s3, v7
	s_nop 3
	s_lshl_b32 s2, s2, 21
	s_add_u32 s8, s84, s2
	s_addc_u32 s9, s85, 0
	s_add_u32 s12, s8, 0x1c000000
	s_addc_u32 s13, s9, 0
	s_add_u32 s8, s8, 0x1e000000
	s_addc_u32 s9, s9, 0
	s_add_u32 s10, s66, s2
	s_addc_u32 s11, s67, 0
	s_add_u32 s10, s10, 0x2000000
	s_addc_u32 s11, s11, 0
	s_mov_b32 s14, s3
	s_add_u32 m0, s14, 0x0
	s_nop 0
	global_load_lds_dwordx4 v8, s[8:9]
	s_add_u32 m0, s14, 0x400
	s_nop 0
	global_load_lds_dwordx4 v9, s[8:9]
	s_add_u32 m0, s14, 0x800
	s_nop 0
	global_load_lds_dwordx4 v10, s[8:9]
	s_add_u32 m0, s14, 0xc00
	s_nop 0
	global_load_lds_dwordx4 v11, s[8:9]
	s_add_u32 m0, s14, 0x4000
	s_nop 0
	global_load_lds_dwordx4 v8, s[10:11]
	s_add_u32 m0, s14, 0x4400
	s_nop 0
	global_load_lds_dwordx4 v9, s[10:11]
	s_add_u32 m0, s14, 0x4800
	s_nop 0
	global_load_lds_dwordx4 v10, s[10:11]
	s_add_u32 m0, s14, 0x4c00
	s_nop 0
	global_load_lds_dwordx4 v11, s[10:11]
	s_add_u32 m0, s14, 0x8000
	s_nop 0
	global_load_lds_dwordx4 v3, s[12:13]
	s_add_u32 m0, s14, 0x8400
	s_nop 0
	global_load_lds_dwordx4 v4, s[12:13]
	s_add_u32 m0, s14, 0x8800
	s_nop 0
	global_load_lds_dwordx4 v5, s[12:13]
	s_add_u32 m0, s14, 0x8c00
	s_nop 0
	global_load_lds_dwordx4 v6, s[12:13]
	s_add_u32 s8, s8, 0x4000
	s_addc_u32 s9, s9, 0
	s_add_u32 s10, s10, 0x4000
	s_addc_u32 s11, s11, 0
	s_add_u32 s12, s12, 0x4000
	s_addc_u32 s13, s13, 0
	s_add_u32 s14, s3, 0xc000
	s_add_u32 m0, s14, 0x0
	s_nop 0
	global_load_lds_dwordx4 v8, s[8:9]
	s_add_u32 m0, s14, 0x400
	s_nop 0
	global_load_lds_dwordx4 v9, s[8:9]
	s_add_u32 m0, s14, 0x800
	s_nop 0
	global_load_lds_dwordx4 v10, s[8:9]
	s_add_u32 m0, s14, 0xc00
	s_nop 0
	global_load_lds_dwordx4 v11, s[8:9]
	s_add_u32 m0, s14, 0x4000
	s_nop 0
	global_load_lds_dwordx4 v8, s[10:11]
	s_add_u32 m0, s14, 0x4400
	s_nop 0
	global_load_lds_dwordx4 v9, s[10:11]
	s_add_u32 m0, s14, 0x4800
	s_nop 0
	global_load_lds_dwordx4 v10, s[10:11]
	s_add_u32 m0, s14, 0x4c00
	s_nop 0
	global_load_lds_dwordx4 v11, s[10:11]
	s_add_u32 m0, s14, 0x8000
	s_nop 0
	global_load_lds_dwordx4 v3, s[12:13]
	s_add_u32 m0, s14, 0x8400
	s_nop 0
	global_load_lds_dwordx4 v4, s[12:13]
	s_add_u32 m0, s14, 0x8800
	s_nop 0
	global_load_lds_dwordx4 v5, s[12:13]
	s_add_u32 m0, s14, 0x8c00
	s_nop 0
	global_load_lds_dwordx4 v6, s[12:13]
	s_add_u32 s8, s8, 0x4000
	s_addc_u32 s9, s9, 0
	s_add_u32 s10, s10, 0x4000
	s_addc_u32 s11, s11, 0
	s_add_u32 s12, s12, 0x4000
	s_addc_u32 s13, s13, 0
	s_add_u32 s14, s3, 0x18000
	s_mov_b32 s2, 0
	s_barrier
.Lshadow_loop:
	s_cmp_eq_u32 s2, 0x7f
	s_cbranch_scc1 .Lshadow_last
	s_waitcnt vmcnt(12)
	s_barrier
	s_cmp_gt_u32 s2, 0x7d
	s_cbranch_scc1 .Lshadow_noissue
	s_add_u32 m0, s14, 0x0
	s_nop 0
	global_load_lds_dwordx4 v8, s[8:9]
	s_add_u32 m0, s14, 0x400
	s_nop 0
	global_load_lds_dwordx4 v9, s[8:9]
	s_add_u32 m0, s14, 0x800
	s_nop 0
	global_load_lds_dwordx4 v10, s[8:9]
	s_add_u32 m0, s14, 0xc00
	s_nop 0
	global_load_lds_dwordx4 v11, s[8:9]
	s_add_u32 m0, s14, 0x4000
	s_nop 0
	global_load_lds_dwordx4 v8, s[10:11]
	s_add_u32 m0, s14, 0x4400
	s_nop 0
	global_load_lds_dwordx4 v9, s[10:11]
	s_add_u32 m0, s14, 0x4800
	s_nop 0
	global_load_lds_dwordx4 v10, s[10:11]
	s_add_u32 m0, s14, 0x4c00
	s_nop 0
	global_load_lds_dwordx4 v11, s[10:11]
	s_add_u32 m0, s14, 0x8000
	s_nop 0
	global_load_lds_dwordx4 v3, s[12:13]
	s_add_u32 m0, s14, 0x8400
	s_nop 0
	global_load_lds_dwordx4 v4, s[12:13]
	s_add_u32 m0, s14, 0x8800
	s_nop 0
	global_load_lds_dwordx4 v5, s[12:13]
	s_add_u32 m0, s14, 0x8c00
	s_nop 0
	global_load_lds_dwordx4 v6, s[12:13]
	s_add_u32 s8, s8, 0x4000
	s_addc_u32 s9, s9, 0
	s_add_u32 s10, s10, 0x4000
	s_addc_u32 s11, s11, 0
	s_add_u32 s12, s12, 0x4000
	s_addc_u32 s13, s13, 0
	s_add_u32 s14, s14, 0xc000
	s_add_u32 s15, s3, 0x24000
	s_cmp_eq_u32 s14, s15
	s_cselect_b32 s14, s3, s14
.Lshadow_noissue:
	s_add_u32 s2, s2, 1
	s_branch .Lshadow_loop
.Lshadow_last:
	s_waitcnt vmcnt(0)
	s_barrier
	s_barrier
.LBB0_1212:
	s_andn2_saveexec_b64 s[2:3], s[6:7]
	s_cbranch_execz .LBB0_1226
	v_readlane_b32 s2, v250, 0
	v_lshrrev_b32_e32 v0, 6, v206
	v_and_b32_e32 v1, 63, v206
	v_lshlrev_b32_e32 v130, 4, v1
	v_lshl_add_u32 v129, v0, 12, v130
	v_lshl_add_u32 v128, v0, 13, v130
	s_nop 3
	s_lshl_b32 s3, s2, 9
	s_add_u32 s12, s84, s3
	s_addc_u32 s13, s85, 0
	s_add_u32 s12, s12, 0x1a00000
	s_addc_u32 s13, s13, 0
	v_cmp_gt_u32_e32 vcc, 0x80, v206
	s_and_saveexec_b64 s[6:7], vcc
	s_cbranch_execz .Lscan_glt_done
	v_lshlrev_b32_e32 v2, 2, v206
	global_load_dword v3, v2, s[12:13]
	v_add_u32_e32 v2, 0x24040, v2
	s_waitcnt vmcnt(0)
	ds_write_b32 v2, v3
; DI float bflo(unsigned u) { return __uint_as_float(u << 16); }
; DI float bfhi(unsigned u) { return __uint_as_float(u & 0xffff0000u); }
; DI bf16x8 packS(const f32x16& x, int s) { return pack8(x[8 * s], x[8 * s + 1], x[8 * s + 2], x[8 * s + 3], x[8 * s + 4], x[8 * s + 5], x[8 * s + 6], x[8 * s + 7]); }
; #define SCAN_RDW(F, mh) do { _Pragma("unroll") for (int k = 0; k < 8; ++k) { const int i2 = k >> 2, m = 2 * (mh) + ((k >> 1) & 1), sx = k & 1; F[k] = *(const bf16x8*)(lw + ((i2 * 4 + m) * 2 + sx) * 1024); } } while (0)
; DI void gdn_scan_seq(const Params& p, int bh16, char* ldsf) {
;     ...
;   f32x16 S[4];
; #pragma unroll
;   for (int m = 0; m < 4; ++m)
; #pragma unroll
;     for (int r = 0; r < 16; ++r) S[m][r] = 0.f;
;   asm volatile("s_waitcnt vmcnt(0)" ::: "memory");
;   __syncthreads();
;   SCAN_ISSUE(0, 0); SCAN_ISSUE(1, 1);
;   int sl = 0;
; #pragma unroll 1
;   for (int c = 0; c < 128; ++c) {
;     if (c + 1 < 128) asm volatile("s_waitcnt vmcnt(12)" ::: "memory"); else asm volatile("s_waitcnt vmcnt(0)" ::: "memory");
;     __builtin_amdgcn_s_barrier();
;     asm volatile("" ::: "memory");
;     char* sco = scp + (size_t)c * 32768;
;     bf16x8 Sb[4][2];
; #pragma unroll
;     for (int m = 0; m < 4; ++m) { Sb[m][0] = packS(S[m], 0); Sb[m][1] = packS(S[m], 1); *(bf16x8*)(sco + (m * 2 + 0) * 1024) = Sb[m][0]; *(bf16x8*)(sco + (m * 2 + 1) * 1024) = Sb[m][1]; }
;     __builtin_amdgcn_sched_barrier(0);
;     if (c + 2 < 128) { const int s2 = sl >= 1 ? sl - 1 : 2; SCAN_ISSUE(c + 2, s2); }
;     const char* base = ldsf + sl * 49152;
;     const char* lw = base + lane * 16; const char* lk = lw + 16384; const char* lu = base + 32768 + wv * 4096 + lane * 16;
;     const float gl = glt[c];
;     f32x16 vn[2];
; #pragma unroll
;     for (int i2 = 0; i2 < 2; ++i2) {
;       const u32x4 ua = *(const u32x4*)(lu + (2 * i2) * 1024), ub = *(const u32x4*)(lu + (2 * i2 + 1) * 1024);
; #pragma unroll
;       for (int e = 0; e < 4; ++e) { vn[i2][2 * e] = bflo(ua[e]); vn[i2][2 * e + 1] = bfhi(ua[e]); vn[i2][8 + 2 * e] = bflo(ub[e]); vn[i2][8 + 2 * e + 1] = bfhi(ub[e]); }
;     }
;     bf16x8 fa[8], fb[8];
;     ...
;     SCAN_RDW(fa, 0);
;     __builtin_amdgcn_sched_barrier(0);
;     SCAN_RDW(fb, 1);
;     __builtin_amdgcn_sched_barrier(0);
;     SCAN_MMW(fa, 0);
;     __builtin_amdgcn_sched_barrier(0);
;     SCAN_RDK(fa, 0);
.Lscan_glt_done:
	s_or_b64 exec, exec, s[6:7]
	s_lshl_b32 s3, s2, 22
	s_add_u32 s8, s56, s3
	s_addc_u32 s9, s57, 0
	s_add_u32 s10, s8, 0x1000
	s_addc_u32 s11, s9, 0
	v_mov_b32_e32 v0, 0
	v_mov_b32_e32 v1, 0
	v_mov_b32_e32 v2, 0
	v_mov_b32_e32 v3, 0
	v_mov_b32_e32 v4, 0
	v_mov_b32_e32 v5, 0
	v_mov_b32_e32 v6, 0
	v_mov_b32_e32 v7, 0
	v_mov_b32_e32 v8, 0
	v_mov_b32_e32 v9, 0
	v_mov_b32_e32 v10, 0
	v_mov_b32_e32 v11, 0
	v_mov_b32_e32 v12, 0
	v_mov_b32_e32 v13, 0
	v_mov_b32_e32 v14, 0
	v_mov_b32_e32 v15, 0
	v_mov_b32_e32 v16, 0
	v_mov_b32_e32 v17, 0
	v_mov_b32_e32 v18, 0
	v_mov_b32_e32 v19, 0
	v_mov_b32_e32 v20, 0
	v_mov_b32_e32 v21, 0
	v_mov_b32_e32 v22, 0
	v_mov_b32_e32 v23, 0
	v_mov_b32_e32 v24, 0
	v_mov_b32_e32 v25, 0
	v_mov_b32_e32 v26, 0
	v_mov_b32_e32 v27, 0
	v_mov_b32_e32 v28, 0
	v_mov_b32_e32 v29, 0
	v_mov_b32_e32 v30, 0
	v_mov_b32_e32 v31, 0
	v_mov_b32_e32 v32, 0
	v_mov_b32_e32 v33, 0
	v_mov_b32_e32 v34, 0
	v_mov_b32_e32 v35, 0
	v_mov_b32_e32 v36, 0
	v_mov_b32_e32 v37, 0
	v_mov_b32_e32 v38, 0
	v_mov_b32_e32 v39, 0
	v_mov_b32_e32 v40, 0
	v_mov_b32_e32 v41, 0
	v_mov_b32_e32 v42, 0
	v_mov_b32_e32 v43, 0
	v_mov_b32_e32 v44, 0
	v_mov_b32_e32 v45, 0
	v_mov_b32_e32 v46, 0
	v_mov_b32_e32 v47, 0
	v_mov_b32_e32 v48, 0
	v_mov_b32_e32 v49, 0
	v_mov_b32_e32 v50, 0
	v_mov_b32_e32 v51, 0
	v_mov_b32_e32 v52, 0
	v_mov_b32_e32 v53, 0
	v_mov_b32_e32 v54, 0
	v_mov_b32_e32 v55, 0
	v_mov_b32_e32 v56, 0
	v_mov_b32_e32 v57, 0
	v_mov_b32_e32 v58, 0
	v_mov_b32_e32 v59, 0
	v_mov_b32_e32 v60, 0
	v_mov_b32_e32 v61, 0
	v_mov_b32_e32 v62, 0
	v_mov_b32_e32 v63, 0
	v_mov_b32_e32 v80, 0
	v_mov_b32_e32 v81, 0
	v_mov_b32_e32 v82, 0
	v_mov_b32_e32 v83, 0
	v_mov_b32_e32 v84, 0
	v_mov_b32_e32 v85, 0
	v_mov_b32_e32 v86, 0
	v_mov_b32_e32 v87, 0
	v_mov_b32_e32 v182, 0
	v_mov_b32_e32 v183, 0
	v_mov_b32_e32 v184, 0
	v_mov_b32_e32 v185, 0
	v_mov_b32_e32 v190, 0
	v_mov_b32_e32 v191, 0
	v_mov_b32_e32 v192, 0
	v_mov_b32_e32 v193, 0
	v_mov_b32_e32 v194, 0
	v_mov_b32_e32 v195, 0
	v_mov_b32_e32 v196, 0
	v_mov_b32_e32 v197, 0
	v_mov_b32_e32 v198, 0
	v_mov_b32_e32 v199, 0
	v_mov_b32_e32 v200, 0
	v_mov_b32_e32 v201, 0
	v_mov_b32_e32 v202, 0
	v_mov_b32_e32 v203, 0
	v_mov_b32_e32 v204, 0
	v_mov_b32_e32 v205, 0
	v_mov_b32_e32 v208, 0
	v_mov_b32_e32 v209, 0
	v_mov_b32_e32 v210, 0
	v_mov_b32_e32 v211, 0
	v_mov_b32_e32 v212, 0
	v_mov_b32_e32 v213, 0
	v_mov_b32_e32 v214, 0
	v_mov_b32_e32 v215, 0
	v_mov_b32_e32 v216, 0
	v_mov_b32_e32 v217, 0
	v_mov_b32_e32 v218, 0
	v_mov_b32_e32 v219, 0
	s_mov_b32 s2, 0
	s_mov_b32 s3, 0
	s_mov_b32 s18, 0x24040
	s_waitcnt lgkmcnt(0)
	s_barrier
.Lscan_loop:
	s_barrier
	v_add_u32_e32 v131, s3, v130
	v_add_u32_e32 v134, s3, v129
	v_mov_b32_e32 v143, s18
	ds_read_b128 v[72:75], v134 offset:32768
	ds_read_b128 v[76:79], v134 offset:33792
	ds_read_b32 v142, v143
	ds_read_b128 v[148:151], v131 offset:0
	ds_read_b128 v[152:155], v131 offset:1024
	ds_read_b128 v[156:159], v131 offset:2048
	ds_read_b128 v[160:163], v131 offset:3072
	ds_read_b128 v[164:167], v131 offset:4096
	ds_read_b128 v[168:171], v131 offset:5120
	ds_read_b128 v[172:175], v131 offset:6144
	ds_read_b128 v[178:181], v131 offset:7168
	ds_read_b128 v[88:91], v134 offset:34816
	ds_read_b128 v[92:95], v134 offset:35840
	s_waitcnt lgkmcnt(10)
	v_mfma_f32_32x32x16_bf16 v[0:15], v[182:185], v[80:83], v[0:15]
	v_lshlrev_b32_e32 v64, 16, v72
	v_and_b32_e32 v65, 0xffff0000, v72
	v_lshlrev_b32_e32 v66, 16, v73
	v_and_b32_e32 v67, 0xffff0000, v73
	v_lshlrev_b32_e32 v68, 16, v74
	v_mfma_f32_32x32x16_bf16 v[0:15], v[190:193], v[84:87], v[0:15]
	v_and_b32_e32 v69, 0xffff0000, v74
	v_lshlrev_b32_e32 v70, 16, v75
	v_and_b32_e32 v71, 0xffff0000, v75
	v_lshlrev_b32_e32 v72, 16, v76
	v_and_b32_e32 v73, 0xffff0000, v76
	v_mfma_f32_32x32x16_bf16 v[16:31], v[194:197], v[80:83], v[16:31]
	v_lshlrev_b32_e32 v74, 16, v77
	v_and_b32_e32 v75, 0xffff0000, v77
	v_lshlrev_b32_e32 v76, 16, v78
	v_and_b32_e32 v77, 0xffff0000, v78
	v_mfma_f32_32x32x16_bf16 v[16:31], v[198:201], v[84:87], v[16:31]
	v_lshlrev_b32_e32 v78, 16, v79
	v_and_b32_e32 v79, 0xffff0000, v79
	s_nop 1
	v_mfma_f32_32x32x16_bf16 v[32:47], v[202:205], v[80:83], v[32:47]
	v_cvt_pk_bf16_f32 v96, v0, v1
	v_cvt_pk_bf16_f32 v97, v2, v3
	v_cvt_pk_bf16_f32 v98, v4, v5
	v_cvt_pk_bf16_f32 v99, v6, v7
	v_cvt_pk_bf16_f32 v100, v8, v9
	v_mfma_f32_32x32x16_bf16 v[32:47], v[208:211], v[84:87], v[32:47]
	v_cvt_pk_bf16_f32 v101, v10, v11
	v_cvt_pk_bf16_f32 v102, v12, v13
	v_cvt_pk_bf16_f32 v103, v14, v15
	s_nop 1
	v_mfma_f32_32x32x16_bf16 v[48:63], v[212:215], v[80:83], v[48:63]
	v_cvt_pk_bf16_f32 v104, v16, v17
	v_cvt_pk_bf16_f32 v105, v18, v19
	v_cvt_pk_bf16_f32 v106, v20, v21
	v_cvt_pk_bf16_f32 v107, v22, v23
	v_cvt_pk_bf16_f32 v108, v24, v25
	v_mfma_f32_32x32x16_bf16 v[48:63], v[216:219], v[84:87], v[48:63]
	v_cvt_pk_bf16_f32 v109, v26, v27
	v_cvt_pk_bf16_f32 v110, v28, v29
	v_cvt_pk_bf16_f32 v111, v30, v31
	s_waitcnt lgkmcnt(0)
; DI float bflo(unsigned u) { return __uint_as_float(u << 16); }
; DI float bfhi(unsigned u) { return __uint_as_float(u & 0xffff0000u); }
; DI bf16x8 packS(const f32x16& x, int s) { return pack8(x[8 * s], x[8 * s + 1], x[8 * s + 2], x[8 * s + 3], x[8 * s + 4], x[8 * s + 5], x[8 * s + 6], x[8 * s + 7]); }
; #define SCAN_RDW(F, mh) do { _Pragma("unroll") for (int k = 0; k < 8; ++k) { const int i2 = k >> 2, m = 2 * (mh) + ((k >> 1) & 1), sx = k & 1; F[k] = *(const bf16x8*)(lw + ((i2 * 4 + m) * 2 + sx) * 1024); } } while (0)
; DI void gdn_scan_seq(const Params& p, int bh16, char* ldsf) {
;     ...
;     char* sco = scp + (size_t)c * 32768;
;     bf16x8 Sb[4][2];
; #pragma unroll
;     for (int m = 0; m < 4; ++m) { Sb[m][0] = packS(S[m], 0); Sb[m][1] = packS(S[m], 1); *(bf16x8*)(sco + (m * 2 + 0) * 1024) = Sb[m][0]; *(bf16x8*)(sco + (m * 2 + 1) * 1024) = Sb[m][1]; }
;     __builtin_amdgcn_sched_barrier(0);
;     if (c + 2 < 128) { const int s2 = sl >= 1 ? sl - 1 : 2; SCAN_ISSUE(c + 2, s2); }
;     const char* base = ldsf + sl * 49152;
;     const char* lw = base + lane * 16; const char* lk = lw + 16384; const char* lu = base + 32768 + wv * 4096 + lane * 16;
;     const float gl = glt[c];
;     f32x16 vn[2];
; #pragma unroll
;     for (int i2 = 0; i2 < 2; ++i2) {
;       const u32x4 ua = *(const u32x4*)(lu + (2 * i2) * 1024), ub = *(const u32x4*)(lu + (2 * i2 + 1) * 1024);
; #pragma unroll
;       for (int e = 0; e < 4; ++e) { vn[i2][2 * e] = bflo(ua[e]); vn[i2][2 * e + 1] = bfhi(ua[e]); vn[i2][8 + 2 * e] = bflo(ub[e]); vn[i2][8 + 2 * e + 1] = bfhi(ub[e]); }
;     }
;     bf16x8 fa[8], fb[8];
;     ...
;     SCAN_RDW(fa, 0);
;     __builtin_amdgcn_sched_barrier(0);
;     SCAN_RDW(fb, 1);
;     __builtin_amdgcn_sched_barrier(0);
;     SCAN_MMW(fa, 0);
;     __builtin_amdgcn_sched_barrier(0);
;     SCAN_RDK(fa, 0);
;     __builtin_amdgcn_sched_barrier(0);
;     SCAN_MMW(fb, 1);
;     __builtin_amdgcn_sched_barrier(0);
;     SCAN_RDK(fb, 1);
;     __builtin_amdgcn_sched_barrier(0);
;     bf16x8 Vb[2][2];
; #pragma unroll
;     for (int j2 = 0; j2 < 2; ++j2) { Vb[j2][0] = packS(vn[j2], 0); Vb[j2][1] = packS(vn[j2], 1); }
; #pragma unroll
;     for (int m = 0; m < 4; ++m)
; #pragma unroll
;       for (int r = 0; r < 16; ++r) S[m][r] *= gl;
;     SCAN_MMK(fa, 0);
;     SCAN_MMK(fb, 1);
;     ...
;     asm volatile("s_waitcnt lgkmcnt(0)" ::: "memory");
;     sl = sl == 2 ? 0 : sl + 1;
;   }
	ds_read_b128 v[182:185], v131 offset:8192
	ds_read_b128 v[190:193], v131 offset:9216
	ds_read_b128 v[194:197], v131 offset:10240
	ds_read_b128 v[198:201], v131 offset:11264
	ds_read_b128 v[202:205], v131 offset:12288
	ds_read_b128 v[208:211], v131 offset:13312
	ds_read_b128 v[212:215], v131 offset:14336
	ds_read_b128 v[216:219], v131 offset:15360
	v_mfma_f32_32x32x16_bf16 v[64:79], v[148:151], v[96:99], v[64:79]
	v_cvt_pk_bf16_f32 v112, v32, v33
	v_cvt_pk_bf16_f32 v113, v34, v35
	v_cvt_pk_bf16_f32 v114, v36, v37
	v_cvt_pk_bf16_f32 v115, v38, v39
	v_cvt_pk_bf16_f32 v116, v40, v41
	v_mfma_f32_32x32x16_bf16 v[64:79], v[152:155], v[100:103], v[64:79]
	v_cvt_pk_bf16_f32 v117, v42, v43
	v_cvt_pk_bf16_f32 v118, v44, v45
	v_cvt_pk_bf16_f32 v119, v46, v47
	v_cvt_pk_bf16_f32 v120, v48, v49
	v_cvt_pk_bf16_f32 v121, v50, v51
	v_mfma_f32_32x32x16_bf16 v[64:79], v[156:159], v[104:107], v[64:79]
	v_cvt_pk_bf16_f32 v122, v52, v53
	v_cvt_pk_bf16_f32 v123, v54, v55
	v_cvt_pk_bf16_f32 v124, v56, v57
	v_cvt_pk_bf16_f32 v125, v58, v59
	v_cvt_pk_bf16_f32 v126, v60, v61
	v_mfma_f32_32x32x16_bf16 v[64:79], v[160:163], v[108:111], v[64:79]
	v_cvt_pk_bf16_f32 v127, v62, v63
	v_lshlrev_b32_e32 v80, 16, v88
	v_and_b32_e32 v81, 0xffff0000, v88
	v_lshlrev_b32_e32 v82, 16, v89
	v_and_b32_e32 v83, 0xffff0000, v89
	v_mfma_f32_32x32x16_bf16 v[64:79], v[164:167], v[112:115], v[64:79]
	v_lshlrev_b32_e32 v84, 16, v90
	v_and_b32_e32 v85, 0xffff0000, v90
	v_lshlrev_b32_e32 v86, 16, v91
	v_and_b32_e32 v87, 0xffff0000, v91
	global_store_dwordx4 v128, v[96:99], s[8:9]
	v_mfma_f32_32x32x16_bf16 v[64:79], v[168:171], v[116:119], v[64:79]
	v_lshlrev_b32_e32 v88, 16, v92
	v_and_b32_e32 v89, 0xffff0000, v92
	v_lshlrev_b32_e32 v90, 16, v93
	v_and_b32_e32 v91, 0xffff0000, v93
	global_store_dwordx4 v128, v[100:103], s[8:9] offset:1024
	v_mfma_f32_32x32x16_bf16 v[64:79], v[172:175], v[120:123], v[64:79]
	v_lshlrev_b32_e32 v92, 16, v94
	v_and_b32_e32 v93, 0xffff0000, v94
	v_lshlrev_b32_e32 v94, 16, v95
	v_and_b32_e32 v95, 0xffff0000, v95
	global_store_dwordx4 v128, v[104:107], s[8:9] offset:2048
	v_mfma_f32_32x32x16_bf16 v[64:79], v[178:181], v[124:127], v[64:79]
	v_pk_mul_f32 v[0:1], v[0:1], v[142:143] op_sel_hi:[1,0]
	v_pk_mul_f32 v[2:3], v[2:3], v[142:143] op_sel_hi:[1,0]
	v_pk_mul_f32 v[4:5], v[4:5], v[142:143] op_sel_hi:[1,0]
	v_pk_mul_f32 v[6:7], v[6:7], v[142:143] op_sel_hi:[1,0]
	global_store_dwordx4 v128, v[108:111], s[8:9] offset:3072
	s_waitcnt lgkmcnt(0)
	ds_read_b128 v[148:151], v131 offset:16384
	ds_read_b128 v[152:155], v131 offset:17408
	ds_read_b128 v[156:159], v131 offset:20480
	ds_read_b128 v[160:163], v131 offset:21504
	ds_read_b128 v[164:167], v131 offset:24576
	ds_read_b128 v[168:171], v131 offset:25600
	ds_read_b128 v[172:175], v131 offset:28672
	ds_read_b128 v[178:181], v131 offset:29696
	v_mfma_f32_32x32x16_bf16 v[80:95], v[182:185], v[96:99], v[80:95]
	v_pk_mul_f32 v[8:9], v[8:9], v[142:143] op_sel_hi:[1,0]
	v_pk_mul_f32 v[10:11], v[10:11], v[142:143] op_sel_hi:[1,0]
	v_pk_mul_f32 v[12:13], v[12:13], v[142:143] op_sel_hi:[1,0]
	v_pk_mul_f32 v[14:15], v[14:15], v[142:143] op_sel_hi:[1,0]
	global_store_dwordx4 v128, v[112:115], s[10:11]
	v_mfma_f32_32x32x16_bf16 v[80:95], v[190:193], v[100:103], v[80:95]
	v_pk_mul_f32 v[16:17], v[16:17], v[142:143] op_sel_hi:[1,0]
	v_pk_mul_f32 v[18:19], v[18:19], v[142:143] op_sel_hi:[1,0]
	v_pk_mul_f32 v[20:21], v[20:21], v[142:143] op_sel_hi:[1,0]
	v_pk_mul_f32 v[22:23], v[22:23], v[142:143] op_sel_hi:[1,0]
	global_store_dwordx4 v128, v[116:119], s[10:11] offset:1024
	v_mfma_f32_32x32x16_bf16 v[80:95], v[194:197], v[104:107], v[80:95]
	v_pk_mul_f32 v[24:25], v[24:25], v[142:143] op_sel_hi:[1,0]
	v_pk_mul_f32 v[26:27], v[26:27], v[142:143] op_sel_hi:[1,0]
	v_pk_mul_f32 v[28:29], v[28:29], v[142:143] op_sel_hi:[1,0]
	v_pk_mul_f32 v[30:31], v[30:31], v[142:143] op_sel_hi:[1,0]
	global_store_dwordx4 v128, v[120:123], s[10:11] offset:2048
	v_mfma_f32_32x32x16_bf16 v[80:95], v[198:201], v[108:111], v[80:95]
	v_pk_mul_f32 v[32:33], v[32:33], v[142:143] op_sel_hi:[1,0]
	v_pk_mul_f32 v[34:35], v[34:35], v[142:143] op_sel_hi:[1,0]
	v_pk_mul_f32 v[36:37], v[36:37], v[142:143] op_sel_hi:[1,0]
	v_pk_mul_f32 v[38:39], v[38:39], v[142:143] op_sel_hi:[1,0]
	global_store_dwordx4 v128, v[124:127], s[10:11] offset:3072
	v_mfma_f32_32x32x16_bf16 v[80:95], v[202:205], v[112:115], v[80:95]
	v_pk_mul_f32 v[40:41], v[40:41], v[142:143] op_sel_hi:[1,0]
	v_pk_mul_f32 v[42:43], v[42:43], v[142:143] op_sel_hi:[1,0]
	v_pk_mul_f32 v[44:45], v[44:45], v[142:143] op_sel_hi:[1,0]
	v_pk_mul_f32 v[46:47], v[46:47], v[142:143] op_sel_hi:[1,0]
	v_mfma_f32_32x32x16_bf16 v[80:95], v[208:211], v[116:119], v[80:95]
	v_pk_mul_f32 v[48:49], v[48:49], v[142:143] op_sel_hi:[1,0]
	v_pk_mul_f32 v[50:51], v[50:51], v[142:143] op_sel_hi:[1,0]
	v_pk_mul_f32 v[52:53], v[52:53], v[142:143] op_sel_hi:[1,0]
	v_pk_mul_f32 v[54:55], v[54:55], v[142:143] op_sel_hi:[1,0]
	v_cvt_pk_bf16_f32 v64, v64, v65
	v_mfma_f32_32x32x16_bf16 v[80:95], v[212:215], v[120:123], v[80:95]
	v_pk_mul_f32 v[56:57], v[56:57], v[142:143] op_sel_hi:[1,0]
	v_pk_mul_f32 v[58:59], v[58:59], v[142:143] op_sel_hi:[1,0]
	v_pk_mul_f32 v[60:61], v[60:61], v[142:143] op_sel_hi:[1,0]
	v_pk_mul_f32 v[62:63], v[62:63], v[142:143] op_sel_hi:[1,0]
	v_cvt_pk_bf16_f32 v65, v66, v67
	v_mfma_f32_32x32x16_bf16 v[80:95], v[216:219], v[124:127], v[80:95]
	v_cvt_pk_bf16_f32 v66, v68, v69
	v_cvt_pk_bf16_f32 v67, v70, v71
	v_cvt_pk_bf16_f32 v68, v72, v73
	v_cvt_pk_bf16_f32 v69, v74, v75
	v_cvt_pk_bf16_f32 v70, v76, v77
	v_cvt_pk_bf16_f32 v71, v78, v79
	s_waitcnt lgkmcnt(0)
	ds_read_b128 v[182:185], v131 offset:18432
	ds_read_b128 v[190:193], v131 offset:19456
	ds_read_b128 v[194:197], v131 offset:22528
	ds_read_b128 v[198:201], v131 offset:23552
	ds_read_b128 v[202:205], v131 offset:26624
	ds_read_b128 v[208:211], v131 offset:27648
	ds_read_b128 v[212:215], v131 offset:30720
	ds_read_b128 v[216:219], v131 offset:31744
	v_mfma_f32_32x32x16_bf16 v[0:15], v[148:151], v[64:67], v[0:15]
	s_add_u32 s2, s2, 1
	s_add_u32 s3, s3, 0xc000
	s_add_u32 s18, s18, 4
	v_mfma_f32_32x32x16_bf16 v[0:15], v[152:155], v[68:71], v[0:15]
	s_add_u32 s8, s8, 0x8000
	s_addc_u32 s9, s9, 0
	s_add_u32 s10, s10, 0x8000
	s_addc_u32 s11, s11, 0
	v_mfma_f32_32x32x16_bf16 v[16:31], v[156:159], v[64:67], v[16:31]
	s_cmp_eq_u32 s3, 0x24000
	s_cselect_b32 s3, 0, s3
	v_mfma_f32_32x32x16_bf16 v[16:31], v[160:163], v[68:71], v[16:31]
	v_cvt_pk_bf16_f32 v80, v80, v81
	v_cvt_pk_bf16_f32 v81, v82, v83
	v_mfma_f32_32x32x16_bf16 v[32:47], v[164:167], v[64:67], v[32:47]
	v_cvt_pk_bf16_f32 v82, v84, v85
	v_cvt_pk_bf16_f32 v83, v86, v87
	v_mfma_f32_32x32x16_bf16 v[32:47], v[168:171], v[68:71], v[32:47]
	v_cvt_pk_bf16_f32 v84, v88, v89
	v_cvt_pk_bf16_f32 v85, v90, v91
	v_mfma_f32_32x32x16_bf16 v[48:63], v[172:175], v[64:67], v[48:63]
	v_cvt_pk_bf16_f32 v86, v92, v93
	v_cvt_pk_bf16_f32 v87, v94, v95
	v_mfma_f32_32x32x16_bf16 v[48:63], v[178:181], v[68:71], v[48:63]
	s_cmp_lt_u32 s2, 0x80
	s_waitcnt lgkmcnt(0)
	s_cbranch_scc1 .Lscan_loop
; DI void gdn_scan_seq(const Params& p, int bh16, char* ldsf) {
;     ...
;     asm volatile("s_waitcnt lgkmcnt(0)" ::: "memory");
;     sl = sl == 2 ? 0 : sl + 1;
;   }
;     ...
;   asm volatile("s_waitcnt vmcnt(0)" ::: "memory");
;   __syncthreads();
	s_waitcnt vmcnt(0)
	s_barrier
